# cv1: prologue convert_item (W_cq f32->bf16 with row gain): 16 load-wait-store steps replaced by two batches of 8 (loads together, counted waits, stores together); on top of rt1
# speedup vs baseline: 1.0062x; 1.0062x over previous
; __device__ __forceinline__ void st_bf4(bf16_t* p, f32x4 v) { u32x2 w; w.x = cvt_pk_bf16(v[0], v[1]); w.y = cvt_pk_bf16(v[2], v[3]); *(u32x2*)p = w; }
; __device__ __forceinline__ void convert_item(const float* W, int ldw, int k0, int n0, const float* gain, bf16_t* O, int lane) {
; #pragma unroll
;     for (int i = 0; i < 16; ++i) { const int k = k0 + 4 * i + (lane >> 4), n = n0 + (lane & 15) * 4; const f32x4 v = *(const f32x4*)(W + (size_t)k * ldw + n) * gain[k]; st_bf4(O + (size_t)k * ldw + n, v); }
; }
.LBB0_187:
	s_andn2_b64 vcc, exec, s[50:51]
	s_cbranch_vccnz .LBB0_189
	s_lshl_b64 s[50:51], s[48:49], 22
	s_add_u32 s50, s16, s50
	s_mul_i32 s6, s48, 0xfffea400
	s_addc_u32 s51, s17, s51
	s_add_i32 s6, s35, s6
	s_add_i32 s6, s6, 0x7fffd400
	s_and_b32 s33, s69, 0x3c0
	s_lshl_b32 s54, s48, 10
	s_and_b32 s6, s6, 0x7fffffc0
	s_ashr_i32 s55, s54, 31
	v_or_b32_e32 v6, s33, v68
	s_lshl_b64 s[54:55], s[54:55], 2
	v_or_b32_e32 v4, s6, v65
	v_lshlrev_b32_e32 v0, 2, v6
	v_mov_b32_e32 v1, v71
	v_mov_b32_e32 v5, v71
	s_add_u32 s54, s12, s54
	v_lshl_add_u64 v[0:1], s[50:51], 0, v[0:1]
	v_lshlrev_b64 v[2:3], 12, v[4:5]
	s_addc_u32 s55, s13, s55
	v_lshl_add_u64 v[2:3], v[0:1], 0, v[2:3]
	global_load_dwordx4 v[20:23], v[2:3], off
	v_lshl_add_u64 v[2:3], v[4:5], 2, s[54:55]
	global_load_dword v8, v[2:3], off
	v_mov_b32_e32 v7, v71
	v_lshlrev_b32_e32 v6, 1, v6
	s_mov_b64 s[50:51], 0x1600000
	v_lshl_add_u64 v[6:7], s[4:5], 0, v[6:7]
	v_mov_b32_e32 v15, v71
	v_lshl_add_u64 v[6:7], v[6:7], 0, s[50:51]
	v_readlane_b32 s55, v251, 15
	s_mov_b32 s54, s86
	v_or_b32_e32 v14, 4, v4
	v_mov_b32_e32 v15, v71
	v_lshlrev_b64 v[18:19], 12, v[14:15]
	v_lshl_add_u64 v[18:19], v[0:1], 0, v[18:19]
	global_load_dwordx4 v[24:27], v[18:19], off
	global_load_dword v9, v[2:3], off offset:16
	v_or_b32_e32 v14, 8, v4
	v_mov_b32_e32 v15, v71
	v_lshlrev_b64 v[18:19], 12, v[14:15]
	v_lshl_add_u64 v[18:19], v[0:1], 0, v[18:19]
	global_load_dwordx4 v[28:31], v[18:19], off
	global_load_dword v10, v[2:3], off offset:32
	v_or_b32_e32 v14, 12, v4
	v_mov_b32_e32 v15, v71
	v_lshlrev_b64 v[18:19], 12, v[14:15]
	v_lshl_add_u64 v[18:19], v[0:1], 0, v[18:19]
	global_load_dwordx4 v[32:35], v[18:19], off
	global_load_dword v11, v[2:3], off offset:48
	v_or_b32_e32 v14, 16, v4
	v_mov_b32_e32 v15, v71
	v_lshlrev_b64 v[18:19], 12, v[14:15]
	v_lshl_add_u64 v[18:19], v[0:1], 0, v[18:19]
	global_load_dwordx4 v[36:39], v[18:19], off
	global_load_dword v12, v[2:3], off offset:64
	v_or_b32_e32 v14, 20, v4
	v_mov_b32_e32 v15, v71
	v_lshlrev_b64 v[18:19], 12, v[14:15]
	v_lshl_add_u64 v[18:19], v[0:1], 0, v[18:19]
	global_load_dwordx4 v[40:43], v[18:19], off
	global_load_dword v13, v[2:3], off offset:80
	v_or_b32_e32 v14, 24, v4
	v_mov_b32_e32 v15, v71
	v_lshlrev_b64 v[18:19], 12, v[14:15]
	v_lshl_add_u64 v[18:19], v[0:1], 0, v[18:19]
	global_load_dwordx4 v[44:47], v[18:19], off
	global_load_dword v16, v[2:3], off offset:96
	v_or_b32_e32 v14, 28, v4
	v_mov_b32_e32 v15, v71
	v_lshlrev_b64 v[18:19], 12, v[14:15]
	v_lshl_add_u64 v[18:19], v[0:1], 0, v[18:19]
	global_load_dwordx4 v[48:51], v[18:19], off
	global_load_dword v17, v[2:3], off offset:112
	s_waitcnt vmcnt(14)
	v_mul_f32_e32 v20, v8, v20
	v_mul_f32_e32 v21, v8, v21
	v_mul_f32_e32 v22, v8, v22
	v_mul_f32_e32 v23, v8, v23
	v_cvt_pk_bf16_f32 v20, v20, v21
	s_nop 0
	v_cvt_pk_bf16_f32 v21, v22, v23
	s_waitcnt vmcnt(12)
	v_mul_f32_e32 v24, v9, v24
	v_mul_f32_e32 v25, v9, v25
	v_mul_f32_e32 v26, v9, v26
	v_mul_f32_e32 v27, v9, v27
	v_cvt_pk_bf16_f32 v24, v24, v25
	s_nop 0
	v_cvt_pk_bf16_f32 v25, v26, v27
	s_waitcnt vmcnt(10)
	v_mul_f32_e32 v28, v10, v28
	v_mul_f32_e32 v29, v10, v29
	v_mul_f32_e32 v30, v10, v30
	v_mul_f32_e32 v31, v10, v31
	v_cvt_pk_bf16_f32 v28, v28, v29
	s_nop 0
	v_cvt_pk_bf16_f32 v29, v30, v31
	s_waitcnt vmcnt(8)
	v_mul_f32_e32 v32, v11, v32
	v_mul_f32_e32 v33, v11, v33
	v_mul_f32_e32 v34, v11, v34
	v_mul_f32_e32 v35, v11, v35
	v_cvt_pk_bf16_f32 v32, v32, v33
	s_nop 0
	v_cvt_pk_bf16_f32 v33, v34, v35
	s_waitcnt vmcnt(6)
	v_mul_f32_e32 v36, v12, v36
	v_mul_f32_e32 v37, v12, v37
	v_mul_f32_e32 v38, v12, v38
	v_mul_f32_e32 v39, v12, v39
	v_cvt_pk_bf16_f32 v36, v36, v37
	s_nop 0
	v_cvt_pk_bf16_f32 v37, v38, v39
	s_waitcnt vmcnt(4)
	v_mul_f32_e32 v40, v13, v40
	v_mul_f32_e32 v41, v13, v41
	v_mul_f32_e32 v42, v13, v42
	v_mul_f32_e32 v43, v13, v43
	v_cvt_pk_bf16_f32 v40, v40, v41
	s_nop 0
	v_cvt_pk_bf16_f32 v41, v42, v43
	s_waitcnt vmcnt(2)
	v_mul_f32_e32 v44, v16, v44
	v_mul_f32_e32 v45, v16, v45
	v_mul_f32_e32 v46, v16, v46
	v_mul_f32_e32 v47, v16, v47
	v_cvt_pk_bf16_f32 v44, v44, v45
	s_nop 0
	v_cvt_pk_bf16_f32 v45, v46, v47
	s_waitcnt vmcnt(0)
; __device__ __forceinline__ void st_bf4(bf16_t* p, f32x4 v) { u32x2 w; w.x = cvt_pk_bf16(v[0], v[1]); w.y = cvt_pk_bf16(v[2], v[3]); *(u32x2*)p = w; }
; __device__ __forceinline__ void convert_item(const float* W, int ldw, int k0, int n0, const float* gain, bf16_t* O, int lane) {
; #pragma unroll
;     for (int i = 0; i < 16; ++i) { const int k = k0 + 4 * i + (lane >> 4), n = n0 + (lane & 15) * 4; const f32x4 v = *(const f32x4*)(W + (size_t)k * ldw + n) * gain[k]; st_bf4(O + (size_t)k * ldw + n, v); }
; }
	v_mul_f32_e32 v48, v17, v48
	v_mul_f32_e32 v49, v17, v49
	v_mul_f32_e32 v50, v17, v50
	v_mul_f32_e32 v51, v17, v51
	v_cvt_pk_bf16_f32 v48, v48, v49
	s_nop 0
	v_cvt_pk_bf16_f32 v49, v50, v51
	v_lshlrev_b64 v[18:19], 11, v[4:5]
	v_lshl_add_u64 v[18:19], v[6:7], 0, v[18:19]
	global_store_dwordx2 v[18:19], v[20:21], off
	v_or_b32_e32 v14, 4, v4
	v_mov_b32_e32 v15, v71
	v_lshlrev_b64 v[18:19], 11, v[14:15]
	v_lshl_add_u64 v[18:19], v[6:7], 0, v[18:19]
	global_store_dwordx2 v[18:19], v[24:25], off
	v_or_b32_e32 v14, 8, v4
	v_mov_b32_e32 v15, v71
	v_lshlrev_b64 v[18:19], 11, v[14:15]
	v_lshl_add_u64 v[18:19], v[6:7], 0, v[18:19]
	global_store_dwordx2 v[18:19], v[28:29], off
	v_or_b32_e32 v14, 12, v4
	v_mov_b32_e32 v15, v71
	v_lshlrev_b64 v[18:19], 11, v[14:15]
	v_lshl_add_u64 v[18:19], v[6:7], 0, v[18:19]
	global_store_dwordx2 v[18:19], v[32:33], off
	v_or_b32_e32 v14, 16, v4
	v_mov_b32_e32 v15, v71
	v_lshlrev_b64 v[18:19], 11, v[14:15]
	v_lshl_add_u64 v[18:19], v[6:7], 0, v[18:19]
	global_store_dwordx2 v[18:19], v[36:37], off
	v_or_b32_e32 v14, 20, v4
	v_mov_b32_e32 v15, v71
	v_lshlrev_b64 v[18:19], 11, v[14:15]
	v_lshl_add_u64 v[18:19], v[6:7], 0, v[18:19]
	global_store_dwordx2 v[18:19], v[40:41], off
	v_or_b32_e32 v14, 24, v4
	v_mov_b32_e32 v15, v71
	v_lshlrev_b64 v[18:19], 11, v[14:15]
	v_lshl_add_u64 v[18:19], v[6:7], 0, v[18:19]
	global_store_dwordx2 v[18:19], v[44:45], off
	v_or_b32_e32 v14, 28, v4
	v_mov_b32_e32 v15, v71
	v_lshlrev_b64 v[18:19], 11, v[14:15]
	v_lshl_add_u64 v[18:19], v[6:7], 0, v[18:19]
	global_store_dwordx2 v[18:19], v[48:49], off
	v_or_b32_e32 v14, 32, v4
	v_mov_b32_e32 v15, v71
	v_lshlrev_b64 v[18:19], 12, v[14:15]
	v_lshl_add_u64 v[18:19], v[0:1], 0, v[18:19]
	global_load_dwordx4 v[20:23], v[18:19], off
	global_load_dword v8, v[2:3], off offset:128
	v_or_b32_e32 v14, 36, v4
	v_mov_b32_e32 v15, v71
	v_lshlrev_b64 v[18:19], 12, v[14:15]
	v_lshl_add_u64 v[18:19], v[0:1], 0, v[18:19]
	global_load_dwordx4 v[24:27], v[18:19], off
	global_load_dword v9, v[2:3], off offset:144
	v_or_b32_e32 v14, 40, v4
	v_mov_b32_e32 v15, v71
	v_lshlrev_b64 v[18:19], 12, v[14:15]
	v_lshl_add_u64 v[18:19], v[0:1], 0, v[18:19]
	global_load_dwordx4 v[28:31], v[18:19], off
	global_load_dword v10, v[2:3], off offset:160
	v_or_b32_e32 v14, 44, v4
	v_mov_b32_e32 v15, v71
	v_lshlrev_b64 v[18:19], 12, v[14:15]
	v_lshl_add_u64 v[18:19], v[0:1], 0, v[18:19]
	global_load_dwordx4 v[32:35], v[18:19], off
	global_load_dword v11, v[2:3], off offset:176
	v_or_b32_e32 v14, 48, v4
	v_mov_b32_e32 v15, v71
	v_lshlrev_b64 v[18:19], 12, v[14:15]
	v_lshl_add_u64 v[18:19], v[0:1], 0, v[18:19]
	global_load_dwordx4 v[36:39], v[18:19], off
	global_load_dword v12, v[2:3], off offset:192
	v_or_b32_e32 v14, 52, v4
	v_mov_b32_e32 v15, v71
	v_lshlrev_b64 v[18:19], 12, v[14:15]
	v_lshl_add_u64 v[18:19], v[0:1], 0, v[18:19]
	global_load_dwordx4 v[40:43], v[18:19], off
	global_load_dword v13, v[2:3], off offset:208
	v_or_b32_e32 v14, 56, v4
	v_mov_b32_e32 v15, v71
	v_lshlrev_b64 v[18:19], 12, v[14:15]
	v_lshl_add_u64 v[18:19], v[0:1], 0, v[18:19]
	global_load_dwordx4 v[44:47], v[18:19], off
	global_load_dword v16, v[2:3], off offset:224
	v_or_b32_e32 v14, 60, v4
	v_mov_b32_e32 v15, v71
	v_lshlrev_b64 v[18:19], 12, v[14:15]
	v_lshl_add_u64 v[18:19], v[0:1], 0, v[18:19]
	global_load_dwordx4 v[48:51], v[18:19], off
	global_load_dword v17, v[2:3], off offset:240
	s_waitcnt vmcnt(14)
	v_mul_f32_e32 v20, v8, v20
	v_mul_f32_e32 v21, v8, v21
	v_mul_f32_e32 v22, v8, v22
	v_mul_f32_e32 v23, v8, v23
	v_cvt_pk_bf16_f32 v20, v20, v21
	s_nop 0
	v_cvt_pk_bf16_f32 v21, v22, v23
	s_waitcnt vmcnt(12)
	v_mul_f32_e32 v24, v9, v24
	v_mul_f32_e32 v25, v9, v25
	v_mul_f32_e32 v26, v9, v26
	v_mul_f32_e32 v27, v9, v27
	v_cvt_pk_bf16_f32 v24, v24, v25
	s_nop 0
	v_cvt_pk_bf16_f32 v25, v26, v27
	s_waitcnt vmcnt(10)
	v_mul_f32_e32 v28, v10, v28
	v_mul_f32_e32 v29, v10, v29
	v_mul_f32_e32 v30, v10, v30
	v_mul_f32_e32 v31, v10, v31
	v_cvt_pk_bf16_f32 v28, v28, v29
	s_nop 0
	v_cvt_pk_bf16_f32 v29, v30, v31
	s_waitcnt vmcnt(8)
	v_mul_f32_e32 v32, v11, v32
	v_mul_f32_e32 v33, v11, v33
	v_mul_f32_e32 v34, v11, v34
	v_mul_f32_e32 v35, v11, v35
	v_cvt_pk_bf16_f32 v32, v32, v33
	s_nop 0
	v_cvt_pk_bf16_f32 v33, v34, v35
	s_waitcnt vmcnt(6)
	v_mul_f32_e32 v36, v12, v36
	v_mul_f32_e32 v37, v12, v37
	v_mul_f32_e32 v38, v12, v38
	v_mul_f32_e32 v39, v12, v39
	v_cvt_pk_bf16_f32 v36, v36, v37
	s_nop 0
	v_cvt_pk_bf16_f32 v37, v38, v39
	s_waitcnt vmcnt(4)
	v_mul_f32_e32 v40, v13, v40
	v_mul_f32_e32 v41, v13, v41
	v_mul_f32_e32 v42, v13, v42
	v_mul_f32_e32 v43, v13, v43
	v_cvt_pk_bf16_f32 v40, v40, v41
	s_nop 0
	v_cvt_pk_bf16_f32 v41, v42, v43
	s_waitcnt vmcnt(2)
	v_mul_f32_e32 v44, v16, v44
	v_mul_f32_e32 v45, v16, v45
	v_mul_f32_e32 v46, v16, v46
	v_mul_f32_e32 v47, v16, v47
	v_cvt_pk_bf16_f32 v44, v44, v45
	s_nop 0
	v_cvt_pk_bf16_f32 v45, v46, v47
	s_waitcnt vmcnt(0)
	v_mul_f32_e32 v48, v17, v48
	v_mul_f32_e32 v49, v17, v49
	v_mul_f32_e32 v50, v17, v50
	v_mul_f32_e32 v51, v17, v51
	v_cvt_pk_bf16_f32 v48, v48, v49
	s_nop 0
	v_cvt_pk_bf16_f32 v49, v50, v51
	v_or_b32_e32 v14, 32, v4
	v_mov_b32_e32 v15, v71
	v_lshlrev_b64 v[18:19], 11, v[14:15]
	v_lshl_add_u64 v[18:19], v[6:7], 0, v[18:19]
	global_store_dwordx2 v[18:19], v[20:21], off
	v_or_b32_e32 v14, 36, v4
	v_mov_b32_e32 v15, v71
	v_lshlrev_b64 v[18:19], 11, v[14:15]
	v_lshl_add_u64 v[18:19], v[6:7], 0, v[18:19]
	global_store_dwordx2 v[18:19], v[24:25], off
	v_or_b32_e32 v14, 40, v4
	v_mov_b32_e32 v15, v71
	v_lshlrev_b64 v[18:19], 11, v[14:15]
	v_lshl_add_u64 v[18:19], v[6:7], 0, v[18:19]
	global_store_dwordx2 v[18:19], v[28:29], off
	v_or_b32_e32 v14, 44, v4
	v_mov_b32_e32 v15, v71
	v_lshlrev_b64 v[18:19], 11, v[14:15]
	v_lshl_add_u64 v[18:19], v[6:7], 0, v[18:19]
	global_store_dwordx2 v[18:19], v[32:33], off
	v_or_b32_e32 v14, 48, v4
	v_mov_b32_e32 v15, v71
	v_lshlrev_b64 v[18:19], 11, v[14:15]
	v_lshl_add_u64 v[18:19], v[6:7], 0, v[18:19]
	global_store_dwordx2 v[18:19], v[36:37], off
	v_or_b32_e32 v14, 52, v4
	v_mov_b32_e32 v15, v71
	v_lshlrev_b64 v[18:19], 11, v[14:15]
	v_lshl_add_u64 v[18:19], v[6:7], 0, v[18:19]
	global_store_dwordx2 v[18:19], v[40:41], off
	v_or_b32_e32 v14, 56, v4
	v_mov_b32_e32 v15, v71
	v_lshlrev_b64 v[18:19], 11, v[14:15]
	v_lshl_add_u64 v[18:19], v[6:7], 0, v[18:19]
	global_store_dwordx2 v[18:19], v[44:45], off
	v_or_b32_e32 v14, 60, v4
	v_mov_b32_e32 v15, v71
	v_lshlrev_b64 v[18:19], 11, v[14:15]
	v_lshl_add_u64 v[18:19], v[6:7], 0, v[18:19]
	global_store_dwordx2 v[18:19], v[48:49], off
